# P2 stage D2 (wave 4 column block): ten serialised tile reads pipelined through a 7-quad ring with counted lgkmcnt; stacked on D1/G/H/I pipelining
# speedup vs baseline: 1.0031x; 1.0031x over previous
.LBB0_454:
	s_andn2_b64 vcc, exec, s[92:93]
	s_cbranch_vccnz .LBB0_456
	v_and_b32_e32 v1, 48, v186
	v_add_u32_e32 v9, v4, v1
	v_lshlrev_b32_e32 v160, 6, v8
	v_add3_u32 v1, s25, v160, v1
	v_lshrrev_b32_e32 v162, 3, v8
	v_lshlrev_b32_e32 v8, 1, v186
	v_and_b32_e32 v163, 14, v8
	s_add_i32 s10, 0, 0x18000
	v_lshlrev_b32_e32 v252, 4, v2
	v_add3_u32 v252, s22, v160, v252
	ds_read_b128 v[228:231], v9 offset:4096
	ds_read_b128 v[232:235], v1 offset:1024
	ds_read_b128 v[236:239], v9 offset:8256
	ds_read_b128 v[240:243], v9 offset:8192
	ds_read_b128 v[244:247], v1 offset:2048
	ds_read_b128 v[248:251], v9 offset:12288
	ds_read_b128 v[10:13], v9 offset:12352
	s_waitcnt lgkmcnt(6)
	v_cvt_pk_bf16_f32 v14, v228, v229
	v_cvt_pk_bf16_f32 v15, v230, v231
	ds_read_b128 v[228:231], v9 offset:12416
	s_waitcnt lgkmcnt(6)
	v_cvt_pk_bf16_f32 v16, v232, v233
	v_cvt_pk_bf16_f32 v17, v234, v235
	ds_read_b128 v[232:235], v1 offset:3072
	s_waitcnt lgkmcnt(6)
	v_cvt_pk_bf16_f32 v6, v236, v237
	v_cvt_pk_bf16_f32 v7, v238, v239
	ds_read_b128 v[236:239], v252
	s_waitcnt lgkmcnt(6)
	v_cvt_pk_bf16_f32 v150, v240, v241
	v_cvt_pk_bf16_f32 v151, v242, v243
	s_waitcnt lgkmcnt(5)
	v_cvt_pk_bf16_f32 v152, v244, v245
	v_cvt_pk_bf16_f32 v153, v246, v247
	s_waitcnt lgkmcnt(4)
	v_cvt_pk_bf16_f32 v4, v248, v249
	v_cvt_pk_bf16_f32 v5, v250, v251
	s_waitcnt lgkmcnt(3)
	v_cvt_pk_bf16_f32 v154, v10, v11
	v_cvt_pk_bf16_f32 v155, v12, v13
	s_waitcnt lgkmcnt(2)
	v_cvt_pk_bf16_f32 v156, v228, v229
	v_cvt_pk_bf16_f32 v157, v230, v231
	s_waitcnt lgkmcnt(1)
	v_cvt_pk_bf16_f32 v158, v232, v233
	v_cvt_pk_bf16_f32 v159, v234, v235
	v_lshlrev_b32_e32 v1, 2, v2
	v_lshlrev_b32_e32 v2, 9, v2
	s_waitcnt lgkmcnt(0)
	v_cvt_pk_bf16_f32 v160, v236, v237
	v_cvt_pk_bf16_f32 v161, v238, v239
	s_nop 1
	v_mfma_f32_16x16x16_bf16 v[8:11], v[14:15], v[160:161], 0
	s_nop 7
	v_cvt_pk_bf16_f32 v8, v8, v9
	v_cvt_pk_bf16_f32 v9, v10, v11
	s_nop 1
	v_mfma_f32_16x16x16_bf16 v[8:11], v[16:17], v[8:9], 0
	s_nop 7
	v_xor_b32_e32 v8, 0x80000000, v8
	v_xor_b32_e32 v9, 0x80000000, v9
	v_bfe_u32 v14, v8, 16, 1
	v_cvt_pk_bf16_f32 v12, v8, v9
	v_add3_u32 v8, v8, v14, s19
	v_and_or_b32 v14, v1, 4, v162
	v_lshl_add_u32 v14, v14, 4, s10
	v_add3_u32 v2, v14, v2, v163
	ds_write_b16_d16_hi v2, v8 offset:2048
	v_or_b32_e32 v8, 17, v1
	v_bfe_u32 v14, v9, 16, 1
	v_add3_u32 v9, v9, v14, s19
	v_lshlrev_b32_e32 v14, 7, v8
	v_bitop3_b32 v8, v8, v162, 5 bitop3:0x6c
	v_lshl_add_u32 v8, v8, 4, s10
	v_xor_b32_e32 v10, 0x80000000, v10
	v_add3_u32 v8, v8, v14, v163
	v_xor_b32_e32 v11, 0x80000000, v11
	ds_write_b16_d16_hi v8, v9
	v_or_b32_e32 v8, 18, v1
	v_bfe_u32 v9, v10, 16, 1
	v_cvt_pk_bf16_f32 v13, v10, v11
	v_add3_u32 v9, v10, v9, s19
	v_lshlrev_b32_e32 v10, 7, v8
	v_and_or_b32 v8, v8, 6, v162
	v_lshl_add_u32 v8, v8, 4, s10
	v_add3_u32 v8, v8, v10, v163
	ds_write_b16_d16_hi v8, v9
	v_or_b32_e32 v8, 19, v1
	v_lshlrev_b32_e32 v10, 7, v8
	v_bitop3_b32 v8, v8, v162, 7 bitop3:0x6c
	v_bfe_u32 v9, v11, 16, 1
	v_lshl_add_u32 v8, v8, 4, s10
	v_add3_u32 v9, v11, v9, s19
	v_add3_u32 v8, v8, v10, v163
	ds_write_b16_d16_hi v8, v9
	v_mfma_f32_16x16x16_bf16 v[8:11], v[150:151], v[160:161], 0
	v_mfma_f32_16x16x16_bf16 v[6:9], v[6:7], v[12:13], v[8:11]
	s_nop 7
	v_cvt_pk_bf16_f32 v6, v6, v7
	v_cvt_pk_bf16_f32 v7, v8, v9
	s_nop 1
	v_mfma_f32_16x16x16_bf16 v[6:9], v[152:153], v[6:7], 0
	s_nop 7
	v_xor_b32_e32 v6, 0x80000000, v6
	v_xor_b32_e32 v7, 0x80000000, v7
	v_bfe_u32 v14, v6, 16, 1
	v_xor_b32_e32 v11, 0x80000000, v8
	v_cvt_pk_bf16_f32 v8, v6, v7
	v_add3_u32 v6, v6, v14, s19
	ds_write_b16_d16_hi v2, v6 offset:4096
	v_or_b32_e32 v6, 33, v1
	v_bfe_u32 v14, v7, 16, 1
	v_add3_u32 v7, v7, v14, s19
	v_lshlrev_b32_e32 v14, 7, v6
	v_bitop3_b32 v6, v6, v162, 5 bitop3:0x6c
	v_lshl_add_u32 v6, v6, 4, s10
	v_add3_u32 v6, v6, v14, v163
	v_xor_b32_e32 v10, 0x80000000, v9
	ds_write_b16_d16_hi v6, v7
	v_or_b32_e32 v6, 34, v1
	v_bfe_u32 v7, v11, 16, 1
	v_cvt_pk_bf16_f32 v9, v11, v10
	v_add3_u32 v7, v11, v7, s19
	v_lshlrev_b32_e32 v11, 7, v6
	v_and_or_b32 v6, v6, 6, v162
	v_lshl_add_u32 v6, v6, 4, s10
	v_add3_u32 v6, v6, v11, v163
	ds_write_b16_d16_hi v6, v7
	v_or_b32_e32 v6, 35, v1
	v_bfe_u32 v7, v10, 16, 1
	v_add3_u32 v7, v10, v7, s19
	v_lshlrev_b32_e32 v10, 7, v6
	v_bitop3_b32 v6, v6, v162, 7 bitop3:0x6c
	v_lshl_add_u32 v6, v6, 4, s10
	v_add3_u32 v6, v6, v10, v163
	ds_write_b16_d16_hi v6, v7
	v_mfma_f32_16x16x16_bf16 v[4:7], v[4:5], v[160:161], 0
	v_mfma_f32_16x16x16_bf16 v[4:7], v[154:155], v[12:13], v[4:7]
	v_mfma_f32_16x16x16_bf16 v[4:7], v[156:157], v[8:9], v[4:7]
	s_nop 7
	v_cvt_pk_bf16_f32 v4, v4, v5
	v_cvt_pk_bf16_f32 v5, v6, v7
	s_nop 1
	v_mfma_f32_16x16x16_bf16 v[4:7], v[158:159], v[4:5], 0
	s_nop 7
	v_xor_b32_e32 v4, 0x80000000, v4
	v_bfe_u32 v8, v4, 16, 1
	v_xor_b32_e32 v5, 0x80000000, v5
	v_add3_u32 v4, v4, v8, s19
	ds_write_b16_d16_hi v2, v4 offset:6144
	v_or_b32_e32 v2, 49, v1
	v_bfe_u32 v4, v5, 16, 1
	v_add3_u32 v4, v5, v4, s19
	v_lshlrev_b32_e32 v5, 7, v2
	v_bitop3_b32 v2, v2, v162, 5 bitop3:0x6c
	v_lshl_add_u32 v2, v2, 4, s10
	v_add3_u32 v2, v2, v5, v163
	ds_write_b16_d16_hi v2, v4
	v_or_b32_e32 v2, 50, v1
	v_xor_b32_e32 v6, 0x80000000, v6
	v_lshlrev_b32_e32 v5, 7, v2
	v_and_or_b32 v2, v2, 6, v162
	v_bfe_u32 v4, v6, 16, 1
	v_lshl_add_u32 v2, v2, 4, s10
	v_add3_u32 v4, v6, v4, s19
	v_add3_u32 v2, v2, v5, v163
	v_or_b32_e32 v1, 51, v1
	v_xor_b32_e32 v7, 0x80000000, v7
	ds_write_b16_d16_hi v2, v4
	v_lshlrev_b32_e32 v4, 7, v1
	v_bitop3_b32 v1, v1, v162, 7 bitop3:0x6c
	v_bfe_u32 v2, v7, 16, 1
	v_lshl_add_u32 v1, v1, 4, s10
	v_add3_u32 v2, v7, v2, s19
	v_add3_u32 v1, v1, v4, v163
	ds_write_b16_d16_hi v1, v2
